# mLSTM S^T stage: all LDS reads hoisted before the MFMAs (Q fragments read once)
# baseline (speedup 1.0000x reference)
; #define LAS __attribute__((address_space(3)))
; __device__ __forceinline__ unsigned long long pack4bf(f32x4 v) { return (unsigned long long)pk2(v[0], v[1]) | ((unsigned long long)pk2(v[2], v[3]) << 32); }
; __device__ __forceinline__ void mlstm_scan_unit(Frame& F, int unit, LAS unsigned* bcnt, unsigned& btarget) {
;     ...
;         { const int tt = w; const int t = 16 * tt + fr; const float mxt = smx[t];
; #pragma unroll
;           for (int jt = 0; jt < 4; ++jt) { f32x4 acc = (f32x4){0.f, 0.f, 0.f, 0.f};
;               if (jt <= tt) {
; #pragma unroll
;                   for (int ks = 0; ks < 4; ++ks) { const s16x8 a = *(const LAS s16x8*)(Lk + (16 * jt + fr) * 136 + 32 * ks + 8 * fq), bq = *(const LAS s16x8*)(Lq + (16 * tt + fr) * 136 + 32 * ks + 8 * fq);
;                       acc = __builtin_amdgcn_mfma_f32_16x16x32_bf16(a, bq, acc, 0, 0, 0); }
;                   const f32x4 u4 = *(const LAS f32x4*)(su + 16 * jt + 4 * fq);
; #pragma unroll
;                   for (int rg_ = 0; rg_ < 4; ++rg_) { const int j = 16 * jt + 4 * fq + rg_; acc[rg_] = (j <= t) ? acc[rg_] * __expf(u4[rg_] - mxt) : 0.f; } }
;               *(LAS unsigned long long*)(Ls + t * 72 + 16 * jt + 4 * fq) = pack4bf(acc); } }
.LBB0_934:
	ds_read_b32 v41, v108
	ds_read_b128 v[164:167], v88 offset:45056
	ds_read_b128 v[168:171], v88 offset:45120
	ds_read_b128 v[172:175], v88 offset:45184
	ds_read_b128 v[176:179], v88 offset:45248
	ds_read_b128 v[180:183], v115 offset:62464
	ds_read_b128 v[184:187], v115 offset:62528
	ds_read_b128 v[188:191], v115 offset:62592
	ds_read_b128 v[192:195], v115 offset:62656
	ds_read_b128 v[72:75], v89
	s_mov_b32 s0, 0x5040100
	v_mov_b32_e32 v152, 0
	v_mov_b32_e32 v153, 0
	v_mov_b32_e32 v154, 0
	v_mov_b32_e32 v155, 0
	v_mov_b32_e32 v156, 0
	v_mov_b32_e32 v157, 0
	v_mov_b32_e32 v158, 0
	v_mov_b32_e32 v159, 0
	v_mov_b32_e32 v148, 0
	v_mov_b32_e32 v149, 0
	v_mov_b32_e32 v150, 0
	v_mov_b32_e32 v151, 0
	s_and_b64 vcc, exec, s[44:45]
	s_cbranch_vccz .Lml_b_rd_done
	ds_read_b128 v[196:199], v116 offset:4352
	ds_read_b128 v[200:203], v116 offset:4416
	ds_read_b128 v[204:207], v116 offset:4480
	ds_read_b128 v[208:211], v116 offset:4544
	ds_read_b128 v[136:139], v89 offset:64
	s_andn2_b64 vcc, exec, s[46:47]
	s_cbranch_vccnz .Lml_b_rd_done
	ds_read_b128 v[212:215], v116 offset:8704
	ds_read_b128 v[216:219], v116 offset:8768
	ds_read_b128 v[220:223], v116 offset:8832
	ds_read_b128 v[224:227], v116 offset:8896
	ds_read_b128 v[140:143], v89 offset:128
	s_andn2_b64 vcc, exec, s[48:49]
	s_cbranch_vccnz .Lml_b_rd_done
	ds_read_b128 v[228:231], v116 offset:13056
	ds_read_b128 v[232:235], v116 offset:13120
	ds_read_b128 v[128:131], v116 offset:13184
	ds_read_b128 v[132:135], v116 offset:13248
	ds_read_b128 v[144:147], v89 offset:192
.Lml_b_rd_done:
	s_waitcnt lgkmcnt(0)
	v_mfma_f32_16x16x32_bf16 v[68:71], v[180:183], v[164:167], 0
	v_mfma_f32_16x16x32_bf16 v[68:71], v[184:187], v[168:171], v[68:71]
	v_mfma_f32_16x16x32_bf16 v[68:71], v[188:191], v[172:175], v[68:71]
	v_mfma_f32_16x16x32_bf16 v[68:71], v[192:195], v[176:179], v[68:71]
	s_and_b64 vcc, exec, s[44:45]
	s_cbranch_vccz .Lml_b_mm_done
	v_mfma_f32_16x16x32_bf16 v[152:155], v[196:199], v[164:167], 0
	v_mfma_f32_16x16x32_bf16 v[152:155], v[200:203], v[168:171], v[152:155]
	v_mfma_f32_16x16x32_bf16 v[152:155], v[204:207], v[172:175], v[152:155]
	v_mfma_f32_16x16x32_bf16 v[152:155], v[208:211], v[176:179], v[152:155]
	s_andn2_b64 vcc, exec, s[46:47]
	s_cbranch_vccnz .Lml_b_mm_done
	v_mfma_f32_16x16x32_bf16 v[156:159], v[212:215], v[164:167], 0
	v_mfma_f32_16x16x32_bf16 v[156:159], v[216:219], v[168:171], v[156:159]
	v_mfma_f32_16x16x32_bf16 v[156:159], v[220:223], v[172:175], v[156:159]
	v_mfma_f32_16x16x32_bf16 v[156:159], v[224:227], v[176:179], v[156:159]
	s_andn2_b64 vcc, exec, s[48:49]
	s_cbranch_vccnz .Lml_b_mm_done
	v_mfma_f32_16x16x32_bf16 v[148:151], v[228:231], v[164:167], 0
	v_mfma_f32_16x16x32_bf16 v[148:151], v[232:235], v[168:171], v[148:151]
	v_mfma_f32_16x16x32_bf16 v[148:151], v[128:131], v[172:175], v[148:151]
	v_mfma_f32_16x16x32_bf16 v[148:151], v[132:135], v[176:179], v[148:151]
.Lml_b_mm_done:
	s_nop 7
	v_sub_f32_e32 v67, v72, v41
	v_mul_f32_e32 v67, 0x3fb8aa3b, v67
	v_exp_f32_e32 v67, v67
	s_nop 2
	v_mul_f32_e32 v67, v68, v67
	v_sub_f32_e32 v68, v73, v41
	v_mul_f32_e32 v68, 0x3fb8aa3b, v68
	v_exp_f32_e32 v68, v68
	v_cndmask_b32_e64 v67, v67, 0, s[6:7]
	v_mul_f32_e32 v68, v69, v68
	v_cndmask_b32_e64 v72, 0, v68, s[8:9]
	v_sub_f32_e32 v68, v74, v41
	v_sub_f32_e32 v69, v75, v41
	v_mul_f32_e32 v68, 0x3fb8aa3b, v68
	v_mul_f32_e32 v69, 0x3fb8aa3b, v69
	v_exp_f32_e32 v68, v68
	v_exp_f32_e32 v69, v69
	s_nop 0
	v_pk_mul_f32 v[68:69], v[70:71], v[68:69]
	v_cvt_pk_bf16_f32 v70, v67, v72
	v_cvt_pk_bf16_f32 v67, v68, v69
	v_cndmask_b32_e64 v68, v67, 0, s[12:13]
	v_lshrrev_b32_e32 v67, 16, v67
	v_cndmask_b32_e64 v67, v67, 0, s[10:11]
	v_perm_b32 v71, v67, v68, s0
	ds_write_b64 v110, v[70:71]
	v_mov_b32_e32 v67, 0
	s_and_b64 vcc, exec, s[44:45]
	s_cbranch_vccz .Lml_b_tail1
	v_sub_f32_e32 v136, v136, v41
	v_sub_f32_e32 v137, v137, v41
	v_sub_f32_e32 v138, v138, v41
	v_sub_f32_e32 v139, v139, v41
	v_mul_f32_e32 v136, 0x3fb8aa3b, v136
	v_mul_f32_e32 v137, 0x3fb8aa3b, v137
	v_mul_f32_e32 v138, 0x3fb8aa3b, v138
	v_mul_f32_e32 v139, 0x3fb8aa3b, v139
	v_exp_f32_e32 v136, v136
	v_exp_f32_e32 v137, v137
	v_exp_f32_e32 v138, v138
	v_exp_f32_e32 v139, v139
	v_pk_mul_f32 v[152:153], v[152:153], v[136:137]
	s_nop 0
	v_cndmask_b32_e64 v152, v152, 0, s[20:21]
	v_pk_mul_f32 v[154:155], v[154:155], v[138:139]
	v_cndmask_b32_e64 v153, v153, 0, s[18:19]
	v_cndmask_b32_e64 v154, v154, 0, s[16:17]
	v_cndmask_b32_e64 v155, v155, 0, s[14:15]
.Lml_b_tail1:
	v_cvt_pk_bf16_f32 v152, v152, v153
	v_cvt_pk_bf16_f32 v153, v154, v155
	ds_write_b64 v110, v[152:153] offset:32
	s_andn2_b64 vcc, exec, s[46:47]
	s_cbranch_vccnz .Lml_b_tail2
	v_sub_f32_e32 v140, v140, v41
	v_sub_f32_e32 v141, v141, v41
	v_sub_f32_e32 v142, v142, v41
	v_sub_f32_e32 v143, v143, v41
	v_mul_f32_e32 v140, 0x3fb8aa3b, v140
	v_mul_f32_e32 v141, 0x3fb8aa3b, v141
	v_mul_f32_e32 v142, 0x3fb8aa3b, v142
	v_mul_f32_e32 v143, 0x3fb8aa3b, v143
	v_exp_f32_e32 v140, v140
	v_exp_f32_e32 v141, v141
	v_exp_f32_e32 v142, v142
	v_exp_f32_e32 v143, v143
	v_pk_mul_f32 v[156:157], v[156:157], v[140:141]
	s_nop 0
	v_cndmask_b32_e64 v156, v156, 0, s[28:29]
	v_pk_mul_f32 v[158:159], v[158:159], v[142:143]
	v_cndmask_b32_e64 v157, v157, 0, s[26:27]
	v_cndmask_b32_e64 v158, v158, 0, s[24:25]
	v_cndmask_b32_e64 v159, v159, 0, s[22:23]
.Lml_b_tail2:
	v_cvt_pk_bf16_f32 v156, v156, v157
	v_cvt_pk_bf16_f32 v157, v158, v159
	ds_write_b64 v110, v[156:157] offset:64
	s_andn2_b64 vcc, exec, s[48:49]
	s_cbranch_vccnz .Lml_b_tail3
	v_sub_f32_e32 v67, v144, v41
	v_mul_f32_e32 v67, 0x3fb8aa3b, v67
	v_exp_f32_e32 v144, v67
	v_sub_f32_e32 v67, v145, v41
	v_mul_f32_e32 v67, 0x3fb8aa3b, v67
	v_exp_f32_e32 v145, v67
	v_sub_f32_e32 v67, v146, v41
	v_sub_f32_e32 v41, v147, v41
	v_mul_f32_e32 v67, 0x3fb8aa3b, v67
	v_mul_f32_e32 v41, 0x3fb8aa3b, v41
	v_exp_f32_e32 v146, v67
	v_exp_f32_e32 v147, v41
	v_pk_mul_f32 v[148:149], v[148:149], v[144:145]
	v_pk_mul_f32 v[150:151], v[150:151], v[146:147]
	v_cndmask_b32_e64 v67, v148, 0, s[38:39]
	v_cndmask_b32_e64 v148, v149, 0, s[36:37]
	v_cndmask_b32_e64 v149, v150, 0, s[34:35]
	v_cndmask_b32_e64 v150, v151, 0, s[30:31]
.Lml_b_tail3:
	v_cvt_pk_bf16_f32 v148, v67, v148
	v_cvt_pk_bf16_f32 v149, v149, v150
	ds_write_b64 v110, v[148:149] offset:96
	s_waitcnt lgkmcnt(0)
	s_and_saveexec_b64 s[58:59], s[4:5]
	s_xor_b64 s[58:59], exec, s[58:59]
	s_cbranch_execz .LBB0_944
	s_mov_b64 s[62:63], exec
	v_mbcnt_lo_u32_b32 v41, s62, 0
	v_mbcnt_hi_u32_b32 v41, s63, v41
	v_cmp_eq_u32_e32 vcc, 0, v41
	s_and_saveexec_b64 s[60:61], vcc
	s_bcnt1_i32_b64 s0, s[62:63]
	v_mov_b32_e32 v41, s67
	v_mov_b32_e32 v67, s0
	ds_add_u32 v41, v67
	s_or_b64 exec, exec, s[60:61]
